# SwiGLU reciprocal merge also in the layer-1 gate/up epilogue (13 of 16 accumulator quads; second pair's exp/1+e moved to a spare register pair), on top of the layer-0 merge
# speedup vs baseline: 1.0010x; 1.0010x over previous
.LBB0_3348:
	s_mov_b32 s82, 0xc2700000
	v_mov_b32_e32 v190, 0x41898193
	v_lshlrev_b32_e32 v160, 16, v46
	v_and_b32_e32 v161, 0xffff0000, v46
	v_lshlrev_b32_e32 v156, 16, v42
	v_and_b32_e32 v157, 0xffff0000, v42
	v_mul_f32_e32 v42, 0x3d800000, v179
	v_lshlrev_b32_e32 v154, 16, v47
	v_and_b32_e32 v155, 0xffff0000, v47
	v_lshlrev_b32_e32 v46, 16, v44
	v_and_b32_e32 v47, 0xffff0000, v44
	v_lshlrev_b32_e32 v150, 16, v45
	v_and_b32_e32 v151, 0xffff0000, v45
	v_pk_fma_f32 v[44:45], v[42:43], v[130:131], v[160:161] op_sel_hi:[0,1,1]
	v_med3_f32 v44, v44, s82, v190
	v_med3_f32 v45, v45, s82, v190
	v_exp_f32_e64 v130, -v44
	v_exp_f32_e64 v131, -v45
	v_pk_fma_f32 v[132:133], v[42:43], v[132:133], v[154:155] op_sel_hi:[0,1,1]
	v_med3_f32 v132, v132, s82, v190
	v_med3_f32 v133, v133, s82, v190
	v_pk_add_f32 v[130:131], v[130:131], 1.0 op_sel_hi:[1,0]
	v_exp_f32_e64 v188, -v132
	v_exp_f32_e64 v189, -v133
	v_lshlrev_b32_e32 v152, 16, v48
	v_and_b32_e32 v153, 0xffff0000, v48
	v_pk_add_f32 v[188:189], v[188:189], 1.0 op_sel_hi:[1,0]
	v_pk_fma_f32 v[122:123], v[42:43], v[122:123], v[152:153] op_sel_hi:[0,1,1]
	v_pk_mul_f32 v[184:185], v[130:131], v[188:189]
	v_rcp_f32_e32 v184, v184
	v_rcp_f32_e32 v185, v185
	s_nop 0
	v_pk_mul_f32 v[186:187], v[184:185], v[188:189]
	v_pk_mul_f32 v[188:189], v[184:185], v[130:131]
	v_pk_mul_f32 v[44:45], v[44:45], v[186:187]
	v_med3_f32 v122, v122, s82, v190
	v_med3_f32 v123, v123, s82, v190
	v_lshlrev_b32_e32 v48, 16, v49
	v_pk_mul_f32 v[130:131], v[132:133], v[188:189]
	v_exp_f32_e64 v132, -v122
	v_exp_f32_e64 v133, -v123
	v_and_b32_e32 v49, 0xffff0000, v49
	v_pk_fma_f32 v[124:125], v[42:43], v[124:125], v[48:49] op_sel_hi:[0,1,1]
	v_lshlrev_b32_e32 v158, 16, v43
	v_and_b32_e32 v159, 0xffff0000, v43
	v_med3_f32 v124, v124, s82, v190
	v_med3_f32 v125, v125, s82, v190
	v_pk_fma_f32 v[136:137], v[42:43], v[136:137], v[158:159] op_sel_hi:[0,1,1]
	v_pk_fma_f32 v[134:135], v[42:43], v[134:135], v[156:157] op_sel_hi:[0,1,1]
	v_pk_fma_f32 v[128:129], v[42:43], v[128:129], v[150:151] op_sel_hi:[0,1,1]
	v_pk_add_f32 v[132:133], v[132:133], 1.0 op_sel_hi:[1,0]
	v_pk_fma_f32 v[42:43], v[42:43], v[126:127], v[46:47] op_sel_hi:[0,1,1]
	v_exp_f32_e64 v188, -v124
	v_exp_f32_e64 v189, -v125
	v_med3_f32 v42, v42, s81, v170
	v_pk_add_f32 v[188:189], v[188:189], 1.0 op_sel_hi:[1,0]
	v_med3_f32 v43, v43, s81, v170
	v_pk_mul_f32 v[184:185], v[132:133], v[188:189]
	v_rcp_f32_e32 v184, v184
	v_rcp_f32_e32 v185, v185
	s_nop 0
	v_pk_mul_f32 v[186:187], v[184:185], v[188:189]
	v_pk_mul_f32 v[188:189], v[184:185], v[132:133]
	v_pk_mul_f32 v[122:123], v[122:123], v[186:187]
	v_pk_mul_f32 v[42:43], v[122:123], v[42:43]
	v_med3_f32 v123, v129, s81, v170
	v_mov_b32_e32 v129, 0
	v_cvt_pk_fp8_f32 v129, v42, v43
	v_med3_f32 v122, v128, s81, v170
	v_pk_mul_f32 v[42:43], v[124:125], v[188:189]
	v_med3_f32 v134, v134, s81, v170
	v_med3_f32 v135, v135, s81, v170
	v_pk_mul_f32 v[42:43], v[42:43], v[122:123]
	v_pk_mul_f32 v[44:45], v[44:45], v[134:135]
	v_mov_b32_e32 v128, 0
	v_cvt_pk_fp8_f32 v129, v42, v43 op_sel:[0,0,1]
	v_mul_f32_e32 v42, 0x3d800000, v178
	v_cvt_pk_fp8_f32 v128, v44, v45
	v_pk_fma_f32 v[44:45], v[42:43], v[114:115], v[160:161] op_sel_hi:[0,1,1]
	v_med3_f32 v44, v44, s82, v190
	v_med3_f32 v45, v45, s82, v190
	v_exp_f32_e64 v114, -v44
	v_exp_f32_e64 v115, -v45
	v_pk_fma_f32 v[116:117], v[42:43], v[116:117], v[154:155] op_sel_hi:[0,1,1]
	v_med3_f32 v116, v116, s82, v190
	v_med3_f32 v117, v117, s82, v190
	v_pk_add_f32 v[114:115], v[114:115], 1.0 op_sel_hi:[1,0]
	v_exp_f32_e64 v188, -v116
	v_exp_f32_e64 v189, -v117
	v_pk_fma_f32 v[106:107], v[42:43], v[106:107], v[152:153] op_sel_hi:[0,1,1]
	v_med3_f32 v106, v106, s82, v190
	v_pk_add_f32 v[188:189], v[188:189], 1.0 op_sel_hi:[1,0]
	v_med3_f32 v107, v107, s82, v190
	v_pk_mul_f32 v[184:185], v[114:115], v[188:189]
	v_rcp_f32_e32 v184, v184
	v_rcp_f32_e32 v185, v185
	s_nop 0
	v_pk_mul_f32 v[186:187], v[184:185], v[188:189]
	v_pk_mul_f32 v[188:189], v[184:185], v[114:115]
	v_pk_mul_f32 v[44:45], v[44:45], v[186:187]
	v_pk_fma_f32 v[108:109], v[42:43], v[108:109], v[48:49] op_sel_hi:[0,1,1]
	v_med3_f32 v108, v108, s82, v190
	v_med3_f32 v109, v109, s82, v190
	v_pk_mul_f32 v[114:115], v[116:117], v[188:189]
	v_exp_f32_e64 v116, -v106
	v_exp_f32_e64 v117, -v107
	v_pk_fma_f32 v[120:121], v[42:43], v[120:121], v[158:159] op_sel_hi:[0,1,1]
	v_pk_fma_f32 v[118:119], v[42:43], v[118:119], v[156:157] op_sel_hi:[0,1,1]
	v_pk_fma_f32 v[112:113], v[42:43], v[112:113], v[150:151] op_sel_hi:[0,1,1]
	v_pk_add_f32 v[116:117], v[116:117], 1.0 op_sel_hi:[1,0]
	v_pk_fma_f32 v[42:43], v[42:43], v[110:111], v[46:47] op_sel_hi:[0,1,1]
	v_exp_f32_e64 v188, -v108
	v_exp_f32_e64 v189, -v109
	v_med3_f32 v118, v118, s81, v170
	v_pk_add_f32 v[188:189], v[188:189], 1.0 op_sel_hi:[1,0]
	v_med3_f32 v119, v119, s81, v170
	v_med3_f32 v42, v42, s81, v170
	v_med3_f32 v43, v43, s81, v170
	v_pk_mul_f32 v[184:185], v[116:117], v[188:189]
	v_rcp_f32_e32 v184, v184
	v_rcp_f32_e32 v185, v185
	s_nop 0
	v_pk_mul_f32 v[186:187], v[184:185], v[188:189]
	v_pk_mul_f32 v[188:189], v[184:185], v[116:117]
	v_pk_mul_f32 v[106:107], v[106:107], v[186:187]
	v_pk_mul_f32 v[44:45], v[44:45], v[118:119]
	v_pk_mul_f32 v[42:43], v[106:107], v[42:43]
	v_med3_f32 v106, v112, s81, v170
	v_med3_f32 v107, v113, s81, v170
	v_mov_b32_e32 v112, 0
	v_mov_b32_e32 v113, 0
	v_mov_b32_e32 v142, v0
	v_cvt_pk_fp8_f32 v112, v44, v45
	v_cvt_pk_fp8_f32 v113, v42, v43
	v_med3_f32 v134, v136, s81, v170
	v_readfirstlane_b32 s65, v142
	v_med3_f32 v135, v137, s81, v170
	s_ashr_i32 s10, s65, 6
	v_pk_mul_f32 v[130:131], v[130:131], v[134:135]
	v_med3_f32 v118, v120, s81, v170
	v_med3_f32 v119, v121, s81, v170
	v_pk_mul_f32 v[42:43], v[108:109], v[188:189]
	s_mul_i32 s11, s10, 0xb00
	v_cvt_pk_fp8_f32 v128, v130, v131 op_sel:[0,0,1]
	v_pk_mul_f32 v[114:115], v[114:115], v[118:119]
	v_pk_mul_f32 v[42:43], v[42:43], v[106:107]
	s_add_i32 s67, s11, 0
	v_and_b32_e32 v147, 15, v142
	v_lshrrev_b32_e32 v125, 1, v142
	v_cvt_pk_fp8_f32 v112, v114, v115 op_sel:[0,0,1]
	v_cvt_pk_fp8_f32 v113, v42, v43 op_sel:[0,0,1]
	s_add_i32 s67, s67, 0x20000
	v_mul_u32_u24_e32 v124, 48, v147
	v_and_b32_e32 v42, 24, v125
	v_add3_u32 v108, s67, v124, v42
	ds_write_b64 v108, v[128:129]
	ds_write_b64 v108, v[112:113] offset:768
	v_mul_f32_e32 v112, 0x3d800000, v177
	v_pk_fma_f32 v[98:99], v[112:113], v[98:99], v[160:161] op_sel_hi:[0,1,1]
	v_med3_f32 v98, v98, s82, v190
	v_med3_f32 v99, v99, s82, v190
	v_exp_f32_e64 v114, -v98
	v_exp_f32_e64 v115, -v99
	v_pk_fma_f32 v[100:101], v[112:113], v[100:101], v[154:155] op_sel_hi:[0,1,1]
	v_med3_f32 v100, v100, s82, v190
	v_med3_f32 v101, v101, s82, v190
	v_pk_add_f32 v[114:115], v[114:115], 1.0 op_sel_hi:[1,0]
	v_exp_f32_e64 v188, -v100
	v_exp_f32_e64 v189, -v101
	v_pk_fma_f32 v[102:103], v[112:113], v[102:103], v[156:157] op_sel_hi:[0,1,1]
	v_pk_fma_f32 v[90:91], v[112:113], v[90:91], v[152:153] op_sel_hi:[0,1,1]
	v_pk_add_f32 v[188:189], v[188:189], 1.0 op_sel_hi:[1,0]
	v_pk_fma_f32 v[104:105], v[112:113], v[104:105], v[158:159] op_sel_hi:[0,1,1]
	v_med3_f32 v102, v102, s81, v170
	v_med3_f32 v103, v103, s81, v170
	v_pk_mul_f32 v[184:185], v[114:115], v[188:189]
	v_rcp_f32_e32 v184, v184
	v_rcp_f32_e32 v185, v185
	s_nop 0
	v_pk_mul_f32 v[186:187], v[184:185], v[188:189]
	v_pk_mul_f32 v[188:189], v[184:185], v[114:115]
	v_pk_mul_f32 v[98:99], v[98:99], v[186:187]
	v_med3_f32 v90, v90, s82, v190
	v_med3_f32 v91, v91, s82, v190
	v_pk_mul_f32 v[98:99], v[98:99], v[102:103]
	v_med3_f32 v102, v104, s81, v170
	v_med3_f32 v103, v105, s81, v170
	v_exp_f32_e64 v104, -v90
	v_exp_f32_e64 v105, -v91
	v_pk_mul_f32 v[100:101], v[100:101], v[188:189]
	v_pk_fma_f32 v[92:93], v[112:113], v[92:93], v[48:49] op_sel_hi:[0,1,1]
	v_pk_mul_f32 v[100:101], v[100:101], v[102:103]
	v_pk_add_f32 v[102:103], v[104:105], 1.0 op_sel_hi:[1,0]
	v_med3_f32 v92, v92, s82, v190
	v_rcp_f32_e32 v102, v102
	v_rcp_f32_e32 v103, v103
	v_med3_f32 v93, v93, s82, v190
	v_pk_fma_f32 v[94:95], v[112:113], v[94:95], v[46:47] op_sel_hi:[0,1,1]
	v_pk_fma_f32 v[96:97], v[112:113], v[96:97], v[150:151] op_sel_hi:[0,1,1]
	v_pk_mul_f32 v[90:91], v[90:91], v[102:103]
	v_exp_f32_e64 v102, -v92
	v_exp_f32_e64 v103, -v93
	v_med3_f32 v94, v94, s81, v170
	v_med3_f32 v95, v95, s81, v170
	v_pk_mul_f32 v[90:91], v[90:91], v[94:95]
	v_med3_f32 v94, v96, s81, v170
	v_med3_f32 v95, v97, s81, v170
	v_pk_add_f32 v[96:97], v[102:103], 1.0 op_sel_hi:[1,0]
	v_mov_b32_e32 v103, v143
	v_rcp_f32_e32 v96, v96
	v_rcp_f32_e32 v97, v97
	v_cvt_pk_fp8_f32 v103, v90, v91
	v_mov_b32_e32 v102, v143
	v_bfe_u32 v106, v142, 1, 5
	v_pk_mul_f32 v[90:91], v[92:93], v[96:97]
	v_lshlrev_b32_e32 v43, 4, v142
	v_pk_mul_f32 v[90:91], v[90:91], v[94:95]
	s_ashr_i32 s65, s65, 2
	v_cvt_pk_fp8_f32 v103, v90, v91 op_sel:[0,0,1]
	v_mul_f32_e32 v90, 0x3d800000, v176
	v_pk_fma_f32 v[82:83], v[90:91], v[82:83], v[160:161] op_sel_hi:[0,1,1]
	v_med3_f32 v82, v82, s82, v190
	v_med3_f32 v83, v83, s82, v190
	v_exp_f32_e64 v92, -v82
	v_exp_f32_e64 v93, -v83
	v_pk_fma_f32 v[84:85], v[90:91], v[84:85], v[154:155] op_sel_hi:[0,1,1]
	v_med3_f32 v84, v84, s82, v190
	v_med3_f32 v85, v85, s82, v190
	v_pk_add_f32 v[92:93], v[92:93], 1.0 op_sel_hi:[1,0]
	v_exp_f32_e64 v188, -v84
	v_exp_f32_e64 v189, -v85
	v_pk_fma_f32 v[86:87], v[90:91], v[86:87], v[156:157] op_sel_hi:[0,1,1]
	v_pk_fma_f32 v[66:67], v[90:91], v[66:67], v[152:153] op_sel_hi:[0,1,1]
	v_pk_add_f32 v[188:189], v[188:189], 1.0 op_sel_hi:[1,0]
	v_pk_fma_f32 v[88:89], v[90:91], v[88:89], v[158:159] op_sel_hi:[0,1,1]
	v_med3_f32 v86, v86, s81, v170
	v_med3_f32 v87, v87, s81, v170
	v_pk_mul_f32 v[184:185], v[92:93], v[188:189]
	v_rcp_f32_e32 v184, v184
	v_rcp_f32_e32 v185, v185
	s_nop 0
	v_pk_mul_f32 v[186:187], v[184:185], v[188:189]
	v_pk_mul_f32 v[188:189], v[184:185], v[92:93]
	v_pk_mul_f32 v[82:83], v[82:83], v[186:187]
	v_med3_f32 v66, v66, s82, v190
	v_med3_f32 v67, v67, s82, v190
	v_pk_mul_f32 v[82:83], v[82:83], v[86:87]
	v_med3_f32 v86, v88, s81, v170
	v_med3_f32 v87, v89, s81, v170
	v_exp_f32_e64 v88, -v66
	v_exp_f32_e64 v89, -v67
	v_pk_mul_f32 v[84:85], v[84:85], v[188:189]
	v_pk_fma_f32 v[68:69], v[90:91], v[68:69], v[48:49] op_sel_hi:[0,1,1]
	v_pk_mul_f32 v[84:85], v[84:85], v[86:87]
	v_pk_add_f32 v[86:87], v[88:89], 1.0 op_sel_hi:[1,0]
	v_med3_f32 v68, v68, s82, v190
	v_rcp_f32_e32 v86, v86
	v_rcp_f32_e32 v87, v87
	v_med3_f32 v69, v69, s82, v190
	v_pk_fma_f32 v[74:75], v[90:91], v[74:75], v[46:47] op_sel_hi:[0,1,1]
	v_pk_fma_f32 v[76:77], v[90:91], v[76:77], v[150:151] op_sel_hi:[0,1,1]
	v_pk_mul_f32 v[66:67], v[66:67], v[86:87]
	v_exp_f32_e64 v86, -v68
	v_exp_f32_e64 v87, -v69
	v_med3_f32 v74, v74, s81, v170
	v_med3_f32 v75, v75, s81, v170
	v_pk_mul_f32 v[66:67], v[66:67], v[74:75]
	v_med3_f32 v74, v76, s81, v170
	v_med3_f32 v75, v77, s81, v170
	v_pk_add_f32 v[76:77], v[86:87], 1.0 op_sel_hi:[1,0]
	v_mov_b32_e32 v87, v143
	v_rcp_f32_e32 v76, v76
	v_rcp_f32_e32 v77, v77
	v_cvt_pk_fp8_f32 v87, v66, v67
	v_cvt_pk_fp8_f32 v102, v98, v99
	v_mov_b32_e32 v86, v143
	v_pk_mul_f32 v[66:67], v[68:69], v[76:77]
	v_mul_f32_e32 v68, 0x3d800000, v175
	v_pk_fma_f32 v[70:71], v[68:69], v[70:71], v[160:161] op_sel_hi:[0,1,1]
	v_med3_f32 v70, v70, s82, v190
	v_med3_f32 v71, v71, s82, v190
	v_pk_mul_f32 v[66:67], v[66:67], v[74:75]
	v_exp_f32_e64 v74, -v70
	v_exp_f32_e64 v75, -v71
	v_pk_fma_f32 v[72:73], v[68:69], v[72:73], v[154:155] op_sel_hi:[0,1,1]
	v_med3_f32 v72, v72, s82, v190
	v_med3_f32 v73, v73, s82, v190
	v_pk_add_f32 v[74:75], v[74:75], 1.0 op_sel_hi:[1,0]
	v_pk_fma_f32 v[76:77], v[68:69], v[80:81], v[158:159] op_sel_hi:[0,1,1]
	v_exp_f32_e64 v188, -v72
	v_exp_f32_e64 v189, -v73
	v_pk_fma_f32 v[58:59], v[68:69], v[58:59], v[152:153] op_sel_hi:[0,1,1]
	v_med3_f32 v58, v58, s82, v190
	v_pk_add_f32 v[188:189], v[188:189], 1.0 op_sel_hi:[1,0]
	v_med3_f32 v59, v59, s82, v190
	v_pk_mul_f32 v[184:185], v[74:75], v[188:189]
	v_rcp_f32_e32 v184, v184
	v_rcp_f32_e32 v185, v185
	s_nop 0
	v_pk_mul_f32 v[186:187], v[184:185], v[188:189]
	v_pk_mul_f32 v[188:189], v[184:185], v[74:75]
	v_pk_mul_f32 v[70:71], v[70:71], v[186:187]
	v_pk_fma_f32 v[60:61], v[68:69], v[60:61], v[48:49] op_sel_hi:[0,1,1]
	v_med3_f32 v60, v60, s82, v190
	v_med3_f32 v61, v61, s82, v190
	v_pk_mul_f32 v[72:73], v[72:73], v[188:189]
	v_exp_f32_e64 v74, -v58
	v_exp_f32_e64 v75, -v59
	v_pk_fma_f32 v[78:79], v[68:69], v[78:79], v[156:157] op_sel_hi:[0,1,1]
	v_pk_fma_f32 v[64:65], v[68:69], v[64:65], v[150:151] op_sel_hi:[0,1,1]
	v_pk_fma_f32 v[62:63], v[68:69], v[62:63], v[46:47] op_sel_hi:[0,1,1]
	v_pk_add_f32 v[74:75], v[74:75], 1.0 op_sel_hi:[1,0]
	v_exp_f32_e64 v188, -v60
	v_exp_f32_e64 v189, -v61
	v_med3_f32 v62, v62, s81, v170
	v_med3_f32 v63, v63, s81, v170
	v_mul_u32_u24_e32 v42, 48, v106
	v_pk_mul_f32 v[58:59], v[58:59], v[62:63]
	v_med3_f32 v62, v64, s81, v170
	v_med3_f32 v63, v65, s81, v170
	v_pk_add_f32 v[188:189], v[188:189], 1.0 op_sel_hi:[1,0]
	v_mov_b32_e32 v69, v143
	v_pk_mul_f32 v[184:185], v[74:75], v[188:189]
	v_rcp_f32_e32 v184, v184
	v_rcp_f32_e32 v185, v185
	s_nop 0
	v_pk_mul_f32 v[186:187], v[184:185], v[188:189]
	v_pk_mul_f32 v[188:189], v[184:185], v[74:75]
	v_pk_mul_f32 v[58:59], v[58:59], v[186:187]
	v_cvt_pk_fp8_f32 v69, v58, v59
	v_and_b32_e32 v142, 16, v43
	s_andn2_b32 s65, s65, 63
	v_pk_mul_f32 v[58:59], v[60:61], v[188:189]
	v_lshl_or_b32 v106, s74, 8, v106
	v_pk_mul_f32 v[58:59], v[58:59], v[62:63]
	v_cvt_pk_fp8_f32 v86, v82, v83
	v_cvt_pk_fp8_f32 v69, v58, v59 op_sel:[0,0,1]
	v_mul_f32_e32 v58, 0x3d800000, v174
	v_pk_fma_f32 v[50:51], v[58:59], v[50:51], v[160:161] op_sel_hi:[0,1,1]
	v_med3_f32 v50, v50, s82, v190
	v_med3_f32 v51, v51, s82, v190
	v_exp_f32_e64 v60, -v50
	v_exp_f32_e64 v61, -v51
	v_pk_fma_f32 v[52:53], v[58:59], v[52:53], v[154:155] op_sel_hi:[0,1,1]
	v_med3_f32 v52, v52, s82, v190
	v_med3_f32 v53, v53, s82, v190
	v_pk_add_f32 v[60:61], v[60:61], 1.0 op_sel_hi:[1,0]
	v_exp_f32_e64 v188, -v52
	v_exp_f32_e64 v189, -v53
	v_pk_fma_f32 v[54:55], v[58:59], v[54:55], v[156:157] op_sel_hi:[0,1,1]
	v_pk_fma_f32 v[34:35], v[58:59], v[34:35], v[152:153] op_sel_hi:[0,1,1]
	v_pk_add_f32 v[188:189], v[188:189], 1.0 op_sel_hi:[1,0]
	v_pk_fma_f32 v[56:57], v[58:59], v[56:57], v[158:159] op_sel_hi:[0,1,1]
	v_med3_f32 v54, v54, s81, v170
	v_med3_f32 v55, v55, s81, v170
	v_pk_mul_f32 v[184:185], v[60:61], v[188:189]
	v_rcp_f32_e32 v184, v184
	v_rcp_f32_e32 v185, v185
	s_nop 0
	v_pk_mul_f32 v[186:187], v[184:185], v[188:189]
	v_pk_mul_f32 v[188:189], v[184:185], v[60:61]
	v_pk_mul_f32 v[50:51], v[50:51], v[186:187]
	v_med3_f32 v34, v34, s82, v190
	v_med3_f32 v35, v35, s82, v190
	v_pk_mul_f32 v[50:51], v[50:51], v[54:55]
	v_med3_f32 v54, v56, s81, v170
	v_med3_f32 v55, v57, s81, v170
	v_exp_f32_e64 v56, -v34
	v_exp_f32_e64 v57, -v35
	v_pk_mul_f32 v[52:53], v[52:53], v[188:189]
	v_pk_fma_f32 v[36:37], v[58:59], v[36:37], v[48:49] op_sel_hi:[0,1,1]
	v_pk_mul_f32 v[52:53], v[52:53], v[54:55]
	v_pk_add_f32 v[54:55], v[56:57], 1.0 op_sel_hi:[1,0]
	v_med3_f32 v36, v36, s82, v190
	v_med3_f32 v37, v37, s82, v190
	s_lshl_b32 s10, s10, 5
	v_add3_u32 v109, s67, v42, v142
	v_add_u32_e32 v106, s65, v106
	v_exp_f32_e64 v188, -v36
	v_exp_f32_e64 v189, -v37
	s_lshl_b32 s11, s76, 7
	s_and_b32 s10, s10, 0x60
	ds_read_b128 v[42:45], v109
	v_ashrrev_i32_e32 v107, 31, v106
	s_or_b32 s10, s10, s11
	v_lshlrev_b64 v[110:111], 10, v[106:107]
	v_cvt_pk_fp8_f32 v102, v100, v101 op_sel:[0,0,1]
	v_pk_fma_f32 v[38:39], v[58:59], v[38:39], v[46:47] op_sel_hi:[0,1,1]
	s_ashr_i32 s11, s10, 31
	v_lshl_add_u64 v[110:111], s[18:19], 0, v[110:111]
	v_cvt_pk_fp8_f32 v86, v84, v85 op_sel:[0,0,1]
	v_cvt_pk_fp8_f32 v87, v66, v67 op_sel:[0,0,1]
	v_pk_fma_f32 v[40:41], v[58:59], v[40:41], v[150:151] op_sel_hi:[0,1,1]
	v_med3_f32 v38, v38, s81, v170
	v_med3_f32 v39, v39, s81, v170
	v_lshl_add_u64 v[110:111], v[110:111], 0, s[10:11]
	v_pk_mul_f32 v[34:35], v[34:35], v[38:39]
	v_med3_f32 v38, v40, s81, v170
	v_med3_f32 v39, v41, s81, v170
	v_pk_add_f32 v[188:189], v[188:189], 1.0 op_sel_hi:[1,0]
	v_lshl_add_u64 v[66:67], v[110:111], 0, v[142:143]
	v_pk_mul_f32 v[184:185], v[54:55], v[188:189]
	v_rcp_f32_e32 v184, v184
	v_rcp_f32_e32 v185, v185
	s_nop 0
	v_pk_mul_f32 v[186:187], v[184:185], v[188:189]
	v_pk_mul_f32 v[188:189], v[184:185], v[54:55]
	v_pk_mul_f32 v[34:35], v[34:35], v[186:187]
	s_waitcnt lgkmcnt(0)
	global_store_dwordx4 v[66:67], v[42:45], off
	ds_write_b64 v108, v[102:103]
	ds_write_b64 v108, v[86:87] offset:768
	v_or_b32_e32 v66, 32, v106
	v_mov_b32_e32 v55, v143
	ds_read_b128 v[42:45], v109
	v_ashrrev_i32_e32 v67, 31, v66
	v_cvt_pk_fp8_f32 v55, v34, v35
	v_lshlrev_b64 v[66:67], 10, v[66:67]
	v_lshl_add_u64 v[66:67], s[18:19], 0, v[66:67]
	v_pk_mul_f32 v[34:35], v[36:37], v[188:189]
	v_mul_f32_e32 v40, 0x3d800000, v171
	v_lshl_add_u64 v[66:67], v[66:67], 0, s[10:11]
	v_pk_mul_f32 v[34:35], v[34:35], v[38:39]
	v_pk_fma_f32 v[26:27], v[40:41], v[26:27], v[160:161] op_sel_hi:[0,1,1]
	v_cvt_pk_fp8_f32 v55, v34, v35 op_sel:[0,0,1]
	v_lshl_add_u64 v[34:35], v[66:67], 0, v[142:143]
	v_med3_f32 v26, v26, s82, v190
	v_med3_f32 v27, v27, s82, v190
	s_waitcnt lgkmcnt(0)
	global_store_dwordx4 v[34:35], v[42:45], off
	v_pk_fma_f32 v[28:29], v[40:41], v[28:29], v[154:155] op_sel_hi:[0,1,1]
	v_med3_f32 v28, v28, s82, v190
	v_exp_f32_e64 v42, -v26
	v_exp_f32_e64 v43, -v27
	v_med3_f32 v29, v29, s82, v190
	v_exp_f32_e64 v188, -v28
	v_exp_f32_e64 v189, -v29
	v_pk_add_f32 v[42:43], v[42:43], 1.0 op_sel_hi:[1,0]
	v_pk_fma_f32 v[30:31], v[40:41], v[30:31], v[156:157] op_sel_hi:[0,1,1]
	v_pk_fma_f32 v[18:19], v[40:41], v[18:19], v[152:153] op_sel_hi:[0,1,1]
	v_pk_fma_f32 v[32:33], v[40:41], v[32:33], v[158:159] op_sel_hi:[0,1,1]
	v_med3_f32 v30, v30, s81, v170
	v_pk_add_f32 v[188:189], v[188:189], 1.0 op_sel_hi:[1,0]
	v_med3_f32 v31, v31, s81, v170
	v_pk_mul_f32 v[184:185], v[42:43], v[188:189]
	v_rcp_f32_e32 v184, v184
	v_rcp_f32_e32 v185, v185
	s_nop 0
	v_pk_mul_f32 v[186:187], v[184:185], v[188:189]
	v_pk_mul_f32 v[188:189], v[184:185], v[42:43]
	v_pk_mul_f32 v[26:27], v[26:27], v[186:187]
	v_med3_f32 v18, v18, s82, v190
	v_med3_f32 v19, v19, s82, v190
	v_pk_mul_f32 v[26:27], v[26:27], v[30:31]
	v_med3_f32 v30, v32, s81, v170
	v_med3_f32 v31, v33, s81, v170
	v_exp_f32_e64 v32, -v18
	v_exp_f32_e64 v33, -v19
	v_pk_mul_f32 v[28:29], v[28:29], v[188:189]
	v_pk_fma_f32 v[20:21], v[40:41], v[20:21], v[48:49] op_sel_hi:[0,1,1]
	v_pk_mul_f32 v[28:29], v[28:29], v[30:31]
	v_pk_add_f32 v[30:31], v[32:33], 1.0 op_sel_hi:[1,0]
	v_med3_f32 v20, v20, s82, v190
	v_rcp_f32_e32 v30, v30
	v_rcp_f32_e32 v31, v31
	v_med3_f32 v21, v21, s82, v190
	v_pk_fma_f32 v[22:23], v[40:41], v[22:23], v[46:47] op_sel_hi:[0,1,1]
	v_pk_fma_f32 v[24:25], v[40:41], v[24:25], v[150:151] op_sel_hi:[0,1,1]
	v_pk_mul_f32 v[18:19], v[18:19], v[30:31]
	v_exp_f32_e64 v30, -v20
	v_exp_f32_e64 v31, -v21
	v_med3_f32 v22, v22, s81, v170
	v_med3_f32 v23, v23, s81, v170
	v_pk_mul_f32 v[18:19], v[18:19], v[22:23]
	v_med3_f32 v22, v24, s81, v170
	v_med3_f32 v23, v25, s81, v170
	v_pk_add_f32 v[24:25], v[30:31], 1.0 op_sel_hi:[1,0]
	v_mov_b32_e32 v31, v143
	v_rcp_f32_e32 v24, v24
	v_rcp_f32_e32 v25, v25
	v_cvt_pk_fp8_f32 v31, v18, v19
	v_med3_f32 v78, v78, s81, v170
	v_med3_f32 v79, v79, s81, v170
	v_pk_mul_f32 v[18:19], v[20:21], v[24:25]
	v_pk_mul_f32 v[70:71], v[70:71], v[78:79]
	v_pk_mul_f32 v[18:19], v[18:19], v[22:23]
	v_mov_b32_e32 v68, v143
	v_cvt_pk_fp8_f32 v31, v18, v19 op_sel:[0,0,1]
	v_mul_f32_e32 v18, 0x3d800000, v169
	v_pk_fma_f32 v[10:11], v[18:19], v[10:11], v[160:161] op_sel_hi:[0,1,1]
	v_med3_f32 v10, v10, s82, v190
	v_med3_f32 v11, v11, s82, v190
	v_exp_f32_e64 v20, -v10
	v_exp_f32_e64 v21, -v11
	v_pk_fma_f32 v[12:13], v[18:19], v[12:13], v[154:155] op_sel_hi:[0,1,1]
	v_med3_f32 v12, v12, s82, v190
	v_med3_f32 v13, v13, s82, v190
	v_pk_add_f32 v[20:21], v[20:21], 1.0 op_sel_hi:[1,0]
	v_exp_f32_e64 v188, -v12
	v_exp_f32_e64 v189, -v13
	v_pk_fma_f32 v[14:15], v[18:19], v[14:15], v[156:157] op_sel_hi:[0,1,1]
	v_pk_fma_f32 v[2:3], v[18:19], v[2:3], v[152:153] op_sel_hi:[0,1,1]
	v_pk_add_f32 v[188:189], v[188:189], 1.0 op_sel_hi:[1,0]
	v_pk_fma_f32 v[16:17], v[18:19], v[16:17], v[158:159] op_sel_hi:[0,1,1]
	v_med3_f32 v14, v14, s81, v170
	v_med3_f32 v15, v15, s81, v170
	v_pk_mul_f32 v[184:185], v[20:21], v[188:189]
	v_rcp_f32_e32 v184, v184
	v_rcp_f32_e32 v185, v185
	s_nop 0
	v_pk_mul_f32 v[186:187], v[184:185], v[188:189]
	v_pk_mul_f32 v[188:189], v[184:185], v[20:21]
	v_pk_mul_f32 v[10:11], v[10:11], v[186:187]
	v_med3_f32 v2, v2, s82, v190
	v_med3_f32 v3, v3, s82, v190
	v_pk_mul_f32 v[10:11], v[10:11], v[14:15]
	v_med3_f32 v14, v16, s81, v170
	v_med3_f32 v15, v17, s81, v170
	v_exp_f32_e64 v16, -v2
	v_exp_f32_e64 v17, -v3
	v_pk_mul_f32 v[12:13], v[12:13], v[188:189]
	v_pk_fma_f32 v[4:5], v[18:19], v[4:5], v[48:49] op_sel_hi:[0,1,1]
	v_pk_mul_f32 v[12:13], v[12:13], v[14:15]
	v_pk_add_f32 v[14:15], v[16:17], 1.0 op_sel_hi:[1,0]
	v_med3_f32 v4, v4, s82, v190
	v_med3_f32 v5, v5, s82, v190
	v_cvt_pk_fp8_f32 v68, v70, v71
	v_mov_b32_e32 v54, v143
	v_exp_f32_e64 v188, -v4
	v_exp_f32_e64 v189, -v5
	v_cvt_pk_fp8_f32 v54, v50, v51
	v_med3_f32 v76, v76, s81, v170
	v_med3_f32 v77, v77, s81, v170
	v_pk_fma_f32 v[6:7], v[18:19], v[6:7], v[46:47] op_sel_hi:[0,1,1]
	v_pk_mul_f32 v[72:73], v[72:73], v[76:77]
	v_pk_fma_f32 v[8:9], v[18:19], v[8:9], v[150:151] op_sel_hi:[0,1,1]
	v_med3_f32 v6, v6, s81, v170
	v_med3_f32 v7, v7, s81, v170
	v_cvt_pk_fp8_f32 v68, v72, v73 op_sel:[0,0,1]
	v_pk_mul_f32 v[2:3], v[2:3], v[6:7]
	v_med3_f32 v6, v8, s81, v170
	v_med3_f32 v7, v9, s81, v170
	v_pk_add_f32 v[188:189], v[188:189], 1.0 op_sel_hi:[1,0]
	v_cvt_pk_fp8_f32 v54, v52, v53 op_sel:[0,0,1]
	v_mov_b32_e32 v30, v143
	v_pk_mul_f32 v[184:185], v[14:15], v[188:189]
	v_rcp_f32_e32 v184, v184
	v_rcp_f32_e32 v185, v185
	s_nop 0
	v_pk_mul_f32 v[186:187], v[184:185], v[188:189]
	v_pk_mul_f32 v[188:189], v[184:185], v[14:15]
	v_pk_mul_f32 v[2:3], v[2:3], v[186:187]
	v_cvt_pk_fp8_f32 v30, v26, v27
	v_mov_b32_e32 v14, v143
	v_mov_b32_e32 v15, v143
	v_cvt_pk_fp8_f32 v14, v10, v11
	v_cvt_pk_fp8_f32 v15, v2, v3
	ds_write_b64 v108, v[68:69]
	ds_write_b64 v108, v[54:55] offset:768
	v_add_u32_e32 v38, 0x80, v106
	ds_read_b128 v[34:37], v109
	v_ashrrev_i32_e32 v39, 31, v38
	v_pk_mul_f32 v[2:3], v[4:5], v[188:189]
	v_lshlrev_b64 v[38:39], 10, v[38:39]
	v_cvt_pk_fp8_f32 v30, v28, v29 op_sel:[0,0,1]
	v_pk_mul_f32 v[2:3], v[2:3], v[6:7]
	v_lshl_add_u64 v[38:39], s[18:19], 0, v[38:39]
	v_cvt_pk_fp8_f32 v14, v12, v13 op_sel:[0,0,1]
	v_cvt_pk_fp8_f32 v15, v2, v3 op_sel:[0,0,1]
	v_lshl_add_u64 v[38:39], v[38:39], 0, s[10:11]
	v_lshl_add_u64 v[2:3], v[38:39], 0, v[142:143]
	s_waitcnt lgkmcnt(0)
	global_store_dwordx4 v[2:3], v[34:37], off
	ds_write_b64 v108, v[30:31]
	ds_write_b64 v108, v[14:15] offset:768
	v_add_u32_e32 v6, 0xa0, v106
	ds_read_b128 v[2:5], v109
	v_ashrrev_i32_e32 v7, 31, v6
	v_lshlrev_b64 v[6:7], 10, v[6:7]
	v_lshl_add_u64 v[6:7], s[18:19], 0, v[6:7]
	v_lshl_add_u64 v[6:7], v[6:7], 0, s[10:11]
	v_lshl_add_u64 v[6:7], v[6:7], 0, v[142:143]
	s_and_b64 vcc, exec, s[8:9]
	s_mov_b64 s[8:9], -1
	s_waitcnt lgkmcnt(0)
	global_store_dwordx4 v[6:7], v[2:5], off
	s_cbranch_vccnz .LBB0_3339
	s_lshl_b64 s[8:9], s[70:71], 12
	s_add_u32 s11, s6, s8
	s_addc_u32 s65, s7, s9
	s_lshl_b32 s8, s64, 7
	s_ashr_i32 s9, s8, 31
	v_mov_b32_e32 v2, v0
	s_lshl_b64 s[8:9], s[8:9], 1
	s_add_u32 s8, s11, s8
	v_readfirstlane_b32 s10, v2
	s_addc_u32 s9, s65, s9
	s_and_b32 s11, s10, 0xc0
	s_add_u32 s8, s8, s11
	s_addc_u32 s9, s9, 0
	v_and_b32_e32 v3, 48, v2
	global_load_dwordx4 v[46:49], v3, s[8:9]
	global_load_dwordx4 v[42:45], v3, s[8:9] offset:2048
	s_ashr_i32 s9, s10, 2
	s_lshl_b32 s8, s66, 8
	s_andn2_b32 s9, s9, 63
	s_add_i32 s9, s9, s8
	v_and_or_b32 v2, v2, 15, s9
	v_ashrrev_i32_e32 v3, 31, v2
	v_lshl_add_u64 v[4:5], v[2:3], 2, s[14:15]
	v_add_u32_e32 v6, 0x80, v2
	v_add_u32_e32 v8, 0x90, v2
	v_add_u32_e32 v10, 0xa0, v2
	v_add_u32_e32 v2, 0xb0, v2
	v_ashrrev_i32_e32 v7, 31, v6
	v_ashrrev_i32_e32 v9, 31, v8
	v_ashrrev_i32_e32 v11, 31, v10
	v_ashrrev_i32_e32 v3, 31, v2
	v_lshl_add_u64 v[6:7], v[6:7], 2, s[14:15]
	v_lshl_add_u64 v[8:9], v[8:9], 2, s[14:15]
	v_lshl_add_u64 v[10:11], v[10:11], 2, s[14:15]
	v_lshl_add_u64 v[2:3], v[2:3], 2, s[14:15]
	global_load_dword v179, v[4:5], off
	global_load_dword v178, v[4:5], off offset:64
	global_load_dword v177, v[4:5], off offset:128
	global_load_dword v176, v[4:5], off offset:192
	global_load_dword v175, v[6:7], off
	global_load_dword v174, v[8:9], off
	global_load_dword v171, v[10:11], off
	global_load_dword v169, v[2:3], off
	s_andn2_b64 vcc, exec, s[16:17]
	s_cbranch_vccnz .LBB0_3338
	s_barrier
	s_branch .LBB0_3338
